# baseline (speedup 1.0000x reference)
.LBB4_18:
.LBB4_24:
	s_and_b64 s[50:51], s[42:43], exec
	s_cselect_b32 s52, s39, s47
	s_cselect_b32 s53, s38, s46
	s_cselect_b32 s54, s41, s45
	s_cselect_b32 s55, s40, s44
	s_add_u32 s28, s46, 0x100
	s_addc_u32 s84, s47, 0
	s_and_b64 s[50:51], s[48:49], exec
	s_cselect_b32 s51, s52, s84
	s_cselect_b32 s50, s53, s28
	s_add_u32 s28, s44, 0x100
	s_addc_u32 s84, s45, 0
	s_and_b64 s[48:49], s[48:49], exec
	s_cselect_b32 s49, s54, s84
	s_cselect_b32 s48, s55, s28
	s_mov_b32 m0, s59
	v_add_u32_e32 v229, s76, v234
	v_lshl_add_u64 v[130:131], s[48:49], 0, v[216:217]
	ds_read_b128 v[74:77], v229
	ds_read_b128 v[86:89], v229 offset:1024
	ds_read_b128 v[98:101], v229 offset:2048
	ds_read_b128 v[106:109], v229 offset:3072
	global_load_lds_dwordx4 v[130:131], off
	v_lshl_add_u64 v[132:133], s[48:49], 0, v[218:219]
	s_mov_b32 m0, s60
	s_nop 0
	global_load_lds_dwordx4 v[132:133], off
	s_barrier
	s_waitcnt lgkmcnt(0)
	s_setprio 1
	s_waitcnt lgkmcnt(0)
	v_mfma_f32_16x16x32_f16 v[94:97], v[74:77], v[46:49], 0
	v_mfma_f32_16x16x32_f16 v[46:49], v[98:101], v[46:49], 0
	v_mfma_f32_16x16x32_f16 v[94:97], v[86:89], v[50:53], v[94:97]
	v_mfma_f32_16x16x32_f16 v[50:53], v[106:109], v[50:53], v[46:49]
	v_mfma_f32_16x16x32_f16 v[46:49], v[74:77], v[38:41], 0
	v_mfma_f32_16x16x32_f16 v[38:41], v[98:101], v[38:41], 0
	v_mfma_f32_16x16x32_f16 v[110:113], v[106:109], v[42:45], v[38:41]
	v_mfma_f32_16x16x32_f16 v[38:41], v[74:77], v[30:33], 0
	v_mfma_f32_16x16x32_f16 v[30:33], v[98:101], v[30:33], 0
	v_mfma_f32_16x16x32_f16 v[174:177], v[106:109], v[34:37], v[30:33]
	v_mfma_f32_16x16x32_f16 v[30:33], v[74:77], v[22:25], 0
	v_mfma_f32_16x16x32_f16 v[22:25], v[98:101], v[22:25], 0
	v_mfma_f32_16x16x32_f16 v[102:105], v[86:89], v[42:45], v[46:49]
	v_mfma_f32_16x16x32_f16 v[170:173], v[86:89], v[34:37], v[38:41]
	v_mfma_f32_16x16x32_f16 v[178:181], v[86:89], v[26:29], v[30:33]
	v_mfma_f32_16x16x32_f16 v[182:185], v[106:109], v[26:29], v[22:25]
	s_setprio 0
	s_mov_b32 m0, s58
	s_barrier
	ds_read_b128 v[34:37], v237 offset:16384
	ds_read_b128 v[46:49], v237 offset:17408
	ds_read_b128 v[114:117], v237 offset:18432
	ds_read_b128 v[118:121], v237 offset:19456
	ds_read_b128 v[122:125], v237 offset:20480
	ds_read_b128 v[126:129], v237 offset:21504
	ds_read_b128 v[166:169], v237 offset:22528
	ds_read_b128 v[186:189], v237 offset:23552
	global_load_lds_dwordx4 v220, s[50:51]
	s_mov_b32 m0, s62
	s_nop 0
	global_load_lds_dwordx4 v226, s[50:51]
	s_barrier
	s_waitcnt lgkmcnt(0)
	s_setprio 1
	s_waitcnt lgkmcnt(0)
	v_mfma_f32_16x16x32_f16 v[22:25], v[6:9], v[34:37], 0
	v_mfma_f32_16x16x32_f16 v[30:33], v[6:9], v[114:117], 0
	v_mfma_f32_16x16x32_f16 v[42:45], v[6:9], v[122:125], 0
	v_mfma_f32_16x16x32_f16 v[6:9], v[6:9], v[166:169], 0
	v_mfma_f32_16x16x32_f16 v[22:25], v[10:13], v[46:49], v[22:25]
	v_mfma_f32_16x16x32_f16 v[26:29], v[14:17], v[34:37], 0
	v_mfma_f32_16x16x32_f16 v[30:33], v[10:13], v[118:121], v[30:33]
	v_mfma_f32_16x16x32_f16 v[38:41], v[14:17], v[114:117], 0
	v_mfma_f32_16x16x32_f16 v[42:45], v[10:13], v[126:129], v[42:45]
	v_mfma_f32_16x16x32_f16 v[134:137], v[14:17], v[122:125], 0
	v_mfma_f32_16x16x32_f16 v[6:9], v[10:13], v[186:189], v[6:9]
	v_mfma_f32_16x16x32_f16 v[10:13], v[14:17], v[166:169], 0
	v_mfma_f32_16x16x32_f16 v[26:29], v[18:21], v[46:49], v[26:29]
	v_mfma_f32_16x16x32_f16 v[38:41], v[18:21], v[118:121], v[38:41]
	v_mfma_f32_16x16x32_f16 v[134:137], v[18:21], v[126:129], v[134:137]
	v_mfma_f32_16x16x32_f16 v[14:17], v[18:21], v[186:189], v[10:13]
	s_setprio 0
	s_barrier
	s_add_u32 s86, s48, 0x40000
	s_addc_u32 s87, s49, 0
	s_add_i32 s84, s76, s57
	v_lshl_add_u64 v[10:11], s[86:87], 0, v[216:217]
	s_mov_b32 m0, s84
	s_add_i32 s85, s84, 0x2000
	global_load_lds_dwordx4 v[10:11], off
	v_lshl_add_u64 v[10:11], s[86:87], 0, v[218:219]
	s_mov_b32 m0, s85
	s_nop 0
	global_load_lds_dwordx4 v[10:11], off
	s_waitcnt vmcnt(6)
	s_barrier
	s_setprio 1
	v_mfma_f32_16x16x32_f16 v[10:13], v[74:77], v[34:37], 0
	v_mfma_f32_16x16x32_f16 v[138:141], v[86:89], v[46:49], v[10:13]
	v_mfma_f32_16x16x32_f16 v[10:13], v[98:101], v[34:37], 0
	v_mfma_f32_16x16x32_f16 v[142:145], v[106:109], v[46:49], v[10:13]
	v_mfma_f32_16x16x32_f16 v[10:13], v[74:77], v[114:117], 0
	v_mfma_f32_16x16x32_f16 v[146:149], v[86:89], v[118:121], v[10:13]
	v_mfma_f32_16x16x32_f16 v[10:13], v[98:101], v[114:117], 0
	v_mfma_f32_16x16x32_f16 v[150:153], v[106:109], v[118:121], v[10:13]
	v_mfma_f32_16x16x32_f16 v[10:13], v[74:77], v[122:125], 0
	v_mfma_f32_16x16x32_f16 v[154:157], v[86:89], v[126:129], v[10:13]
	v_mfma_f32_16x16x32_f16 v[10:13], v[98:101], v[122:125], 0
	v_mfma_f32_16x16x32_f16 v[158:161], v[106:109], v[126:129], v[10:13]
	v_mfma_f32_16x16x32_f16 v[10:13], v[74:77], v[166:169], 0
	v_mfma_f32_16x16x32_f16 v[162:165], v[86:89], v[186:189], v[10:13]
	v_mfma_f32_16x16x32_f16 v[10:13], v[98:101], v[166:169], 0
	v_mfma_f32_16x16x32_f16 v[166:169], v[106:109], v[186:189], v[10:13]
	s_setprio 0
	s_cmp_gt_i32 s61, 44
	s_cbranch_scc1 .Lhka_done_a0
	s_cmp_lt_i32 s61, 1
	s_cbranch_scc1 .Lhka_ld_a0
	s_add_i32 s94, s75, s61
	s_mov_b32 s95, 0
	s_cmpk_gt_u32 s94, 0x15ff
	s_cselect_b32 s97, 0x7fffea00, 0
	s_cselect_b32 s96, 0x80, 0
	s_add_i32 s97, s97, s94
	s_lshl_b32 s94, s97, 1
	s_add_i32 s97, s94, 0x2c00
	s_mul_hi_u32 s98, s97, 0xba2e8ba3
	s_lshr_b32 s98, s98, 11
	s_mul_i32 s99, s98, 0x7ffff500
	s_add_i32 s99, s99, s97
	s_lshr_b32 s97, s99, 7
	s_mul_i32 s98, s98, 22
	s_add_i32 s97, s97, s98
	s_lshl_b32 s97, s97, 8
	s_and_b32 s94, s94, 0x7e
	s_or_b32 s96, s97, s96
	s_or_b32 s94, s96, s94
	s_lshl_b64 s[96:97], s[94:95], 11
	v_cvt_pk_f16_f32 v2, v2, v3
	v_cvt_pk_f16_f32 v3, v4, v5
	v_lshl_add_u64 v[4:5], v[224:225], 0, s[96:97]
	global_store_dwordx2 v[4:5], v[2:3], off

.Lhka_done_a0:
	v_add_u32_e32 v231, 0x18000, v235
	s_barrier
	s_nop 3
	ds_read_b128 v[10:13], v231
	ds_read_b128 v[186:189], v231 offset:1024
	ds_read_b128 v[190:193], v231 offset:2048
	ds_read_b128 v[194:197], v231 offset:3072
	s_mov_b32 m0, s63
	ds_read_b128 v[122:125], v237 offset:32768
	ds_read_b128 v[126:129], v237 offset:33792
	ds_read_b128 v[118:121], v237 offset:34816
	ds_read_b128 v[210:213], v237 offset:35840
	ds_read_b128 v[202:205], v237 offset:36864
	ds_read_b128 v[206:209], v237 offset:37888
	ds_read_b128 v[18:21], v237 offset:38912
	ds_read_b128 v[198:201], v237 offset:39936
	global_load_lds_dwordx4 v228, s[50:51]
	s_mov_b32 m0, s64
	s_nop 0
	global_load_lds_dwordx4 v230, s[50:51]
	s_waitcnt lgkmcnt(8)
	s_barrier
	s_waitcnt lgkmcnt(0)
	s_setprio 1
	s_waitcnt lgkmcnt(0)
	v_mfma_f32_16x16x32_f16 v[34:37], v[10:13], v[122:125], v[54:57]
	v_mfma_f32_16x16x32_f16 v[114:117], v[186:189], v[126:129], v[34:37]
	v_mfma_f32_16x16x32_f16 v[34:37], v[190:193], v[122:125], v[58:61]
	v_mfma_f32_16x16x32_f16 v[106:109], v[194:197], v[126:129], v[34:37]
	v_mfma_f32_16x16x32_f16 v[34:37], v[10:13], v[118:121], v[62:65]
	v_mfma_f32_16x16x32_f16 v[98:101], v[186:189], v[210:213], v[34:37]
	v_mfma_f32_16x16x32_f16 v[34:37], v[190:193], v[118:121], v[66:69]
	v_mfma_f32_16x16x32_f16 v[86:89], v[194:197], v[210:213], v[34:37]
	v_mfma_f32_16x16x32_f16 v[34:37], v[10:13], v[202:205], v[70:73]
	v_mfma_f32_16x16x32_f16 v[74:77], v[186:189], v[206:209], v[34:37]
	v_mfma_f32_16x16x32_f16 v[34:37], v[190:193], v[202:205], v[78:81]
	v_mfma_f32_16x16x32_f16 v[62:65], v[194:197], v[206:209], v[34:37]
	v_mfma_f32_16x16x32_f16 v[34:37], v[10:13], v[18:21], v[82:85]
	v_mfma_f32_16x16x32_f16 v[46:49], v[186:189], v[198:201], v[34:37]
	v_mfma_f32_16x16x32_f16 v[34:37], v[190:193], v[18:21], v[90:93]
	v_mfma_f32_16x16x32_f16 v[34:37], v[194:197], v[198:201], v[34:37]
	s_setprio 0
	s_barrier
.LBB4_30:
	v_mov_b32_e32 v227, v221
	v_lshl_add_u64 v[54:55], s[50:51], 0, v[220:221]
	v_lshl_add_u64 v[56:57], s[50:51], 0, v[226:227]
	s_add_i32 s50, 0, 0x1c000
	s_mov_b32 m0, s67
	v_add_u32_e32 v238, s50, v234
	v_lshl_add_u64 v[58:59], v[130:131], 0, s[30:31]
	ds_read_b128 v[240:243], v238
	ds_read_b128 v[244:247], v238 offset:1024
	ds_read_b128 v[248:251], v238 offset:2048
	ds_read_b128 v[252:255], v238 offset:3072
	global_load_lds_dwordx4 v[58:59], off
	v_lshl_add_u64 v[58:59], v[132:133], 0, s[30:31]
	s_mov_b32 m0, s68
	s_nop 0
	global_load_lds_dwordx4 v[58:59], off
	s_barrier
	s_waitcnt lgkmcnt(0)
	s_setprio 1
	s_waitcnt lgkmcnt(0)
	v_mfma_f32_16x16x32_f16 v[58:61], v[240:243], v[122:125], v[94:97]
	v_mfma_f32_16x16x32_f16 v[50:53], v[248:251], v[122:125], v[50:53]
	v_mfma_f32_16x16x32_f16 v[130:133], v[244:247], v[126:129], v[58:61]
	v_mfma_f32_16x16x32_f16 v[126:129], v[252:255], v[126:129], v[50:53]
	v_mfma_f32_16x16x32_f16 v[50:53], v[240:243], v[118:121], v[102:105]
	v_mfma_f32_16x16x32_f16 v[122:125], v[244:247], v[210:213], v[50:53]
	v_mfma_f32_16x16x32_f16 v[50:53], v[248:251], v[118:121], v[110:113]
	v_mfma_f32_16x16x32_f16 v[118:121], v[252:255], v[210:213], v[50:53]
	v_mfma_f32_16x16x32_f16 v[50:53], v[240:243], v[202:205], v[170:173]
	v_mfma_f32_16x16x32_f16 v[110:113], v[244:247], v[206:209], v[50:53]
	v_mfma_f32_16x16x32_f16 v[50:53], v[248:251], v[202:205], v[174:177]
	v_mfma_f32_16x16x32_f16 v[102:105], v[252:255], v[206:209], v[50:53]
	v_mfma_f32_16x16x32_f16 v[50:53], v[240:243], v[18:21], v[178:181]
	v_mfma_f32_16x16x32_f16 v[18:21], v[248:251], v[18:21], v[182:185]
	v_mfma_f32_16x16x32_f16 v[94:97], v[244:247], v[198:201], v[50:53]
	v_mfma_f32_16x16x32_f16 v[82:85], v[252:255], v[198:201], v[18:21]
	s_setprio 0
	s_mov_b32 m0, s69
	s_nop 3
	v_lshl_add_u64 v[18:19], v[54:55], 0, s[30:31]
	s_barrier
	ds_read_b128 v[66:69], v237 offset:49152
	ds_read_b128 v[78:81], v237 offset:50176
	ds_read_b128 v[170:173], v237 offset:51200
	ds_read_b128 v[174:177], v237 offset:52224
	ds_read_b128 v[178:181], v237 offset:53248
	ds_read_b128 v[182:185], v237 offset:54272
	ds_read_b128 v[198:201], v237 offset:55296
	ds_read_b128 v[202:205], v237 offset:56320
	global_load_lds_dwordx4 v[18:19], off
	v_lshl_add_u64 v[18:19], v[56:57], 0, s[30:31]
	s_mov_b32 m0, s70
	s_nop 0
	global_load_lds_dwordx4 v[18:19], off
	s_barrier
	s_waitcnt lgkmcnt(0)
	s_setprio 1
	s_waitcnt lgkmcnt(0)
	v_mfma_f32_16x16x32_f16 v[18:21], v[10:13], v[66:69], v[22:25]
	v_mfma_f32_16x16x32_f16 v[70:73], v[186:189], v[78:81], v[18:21]
	v_mfma_f32_16x16x32_f16 v[18:21], v[190:193], v[66:69], v[26:29]
	v_mfma_f32_16x16x32_f16 v[58:61], v[194:197], v[78:81], v[18:21]
	v_mfma_f32_16x16x32_f16 v[18:21], v[10:13], v[170:173], v[30:33]
	v_mfma_f32_16x16x32_f16 v[50:53], v[186:189], v[174:177], v[18:21]
	v_mfma_f32_16x16x32_f16 v[18:21], v[190:193], v[170:173], v[38:41]
	v_mfma_f32_16x16x32_f16 v[38:41], v[194:197], v[174:177], v[18:21]
	v_mfma_f32_16x16x32_f16 v[18:21], v[10:13], v[178:181], v[42:45]
	v_mfma_f32_16x16x32_f16 v[6:9], v[10:13], v[198:201], v[6:9]
	v_mfma_f32_16x16x32_f16 v[26:29], v[186:189], v[182:185], v[18:21]
	v_mfma_f32_16x16x32_f16 v[18:21], v[190:193], v[178:181], v[134:137]
	v_mfma_f32_16x16x32_f16 v[10:13], v[186:189], v[202:205], v[6:9]
	v_mfma_f32_16x16x32_f16 v[6:9], v[190:193], v[198:201], v[14:17]
	v_mfma_f32_16x16x32_f16 v[18:21], v[194:197], v[182:185], v[18:21]
	v_mfma_f32_16x16x32_f16 v[6:9], v[194:197], v[202:205], v[6:9]
	s_setprio 0
	s_barrier
	s_add_u32 s48, s48, 0x40080
	s_addc_u32 s49, s49, 0
	s_add_i32 s50, s50, s57
	v_lshl_add_u64 v[14:15], s[48:49], 0, v[216:217]
	s_mov_b32 m0, s50
	s_add_i32 s51, s50, 0x2000
	global_load_lds_dwordx4 v[14:15], off
	v_lshl_add_u64 v[14:15], s[48:49], 0, v[218:219]
	s_mov_b32 m0, s51
	s_nop 0
	global_load_lds_dwordx4 v[14:15], off
	s_waitcnt vmcnt(6)
	s_barrier
	s_setprio 1
	v_mfma_f32_16x16x32_f16 v[14:17], v[240:243], v[66:69], v[138:141]
	v_mfma_f32_16x16x32_f16 v[90:93], v[244:247], v[78:81], v[14:17]
	v_mfma_f32_16x16x32_f16 v[14:17], v[248:251], v[66:69], v[142:145]
	v_mfma_f32_16x16x32_f16 v[78:81], v[252:255], v[78:81], v[14:17]
	v_mfma_f32_16x16x32_f16 v[14:17], v[240:243], v[170:173], v[146:149]
	v_mfma_f32_16x16x32_f16 v[66:69], v[244:247], v[174:177], v[14:17]
	v_mfma_f32_16x16x32_f16 v[14:17], v[248:251], v[170:173], v[150:153]
	v_mfma_f32_16x16x32_f16 v[54:57], v[252:255], v[174:177], v[14:17]
	v_mfma_f32_16x16x32_f16 v[14:17], v[240:243], v[178:181], v[154:157]
	v_mfma_f32_16x16x32_f16 v[42:45], v[244:247], v[182:185], v[14:17]
	v_mfma_f32_16x16x32_f16 v[14:17], v[248:251], v[178:181], v[158:161]
	v_mfma_f32_16x16x32_f16 v[30:33], v[252:255], v[182:185], v[14:17]
	v_mfma_f32_16x16x32_f16 v[14:17], v[240:243], v[198:201], v[162:165]
	v_mfma_f32_16x16x32_f16 v[22:25], v[244:247], v[202:205], v[14:17]
	v_mfma_f32_16x16x32_f16 v[14:17], v[248:251], v[198:201], v[166:169]
	v_mfma_f32_16x16x32_f16 v[14:17], v[252:255], v[202:205], v[14:17]
	s_setprio 0
	s_cmp_gt_i32 s61, 44
	s_cbranch_scc1 .Lhka_done_a1
	s_cmp_lt_i32 s61, 1
	s_cbranch_scc1 .Lhka_ld_a1
	s_add_i32 s94, s75, s61
	s_mov_b32 s95, 0
	s_cmpk_gt_u32 s94, 0x15ff
	s_cselect_b32 s97, 0x7fffea00, 0
	s_cselect_b32 s96, 0x80, 0
	s_add_i32 s97, s97, s94
	s_lshl_b32 s94, s97, 1
	s_add_i32 s97, s94, 0x2c00
	s_mul_hi_u32 s98, s97, 0xba2e8ba3
	s_lshr_b32 s98, s98, 11
	s_mul_i32 s99, s98, 0x7ffff500
	s_add_i32 s99, s99, s97
	s_lshr_b32 s97, s99, 7
	s_mul_i32 s98, s98, 22
	s_add_i32 s97, s97, s98
	s_lshl_b32 s97, s97, 8
	s_and_b32 s94, s94, 0x7e
	s_or_b32 s96, s97, s96
	s_or_b32 s94, s96, s94
	s_lshl_b64 s[96:97], s[94:95], 11
	v_cvt_pk_f16_f32 v2, v2, v3
	v_cvt_pk_f16_f32 v3, v4, v5
	v_lshl_add_u64 v[4:5], v[224:225], 0, s[96:97]
	global_store_dwordx2 v[4:5], v[2:3], off

.Lhka_done_a1:
	s_cmp_lt_u32 s83, 3
	s_barrier
	s_cbranch_scc1 .LBB4_49
	s_add_u32 s46, s46, 0x180
	s_addc_u32 s47, s47, 0
	s_add_u32 s86, s44, 0x200
	s_addc_u32 s87, s45, 0
	s_mov_b32 s88, 4

.LBB4_40:
	s_add_u32 s28, s46, 0x80
	s_addc_u32 s48, s47, 0
	s_and_b64 s[44:45], s[44:45], exec
	s_cselect_b32 s45, s54, s87
	s_cselect_b32 s44, s55, s86
	s_mov_b32 m0, s59
	v_lshl_add_u64 v[182:183], s[44:45], 0, v[216:217]
	ds_read_b128 v[186:189], v229
	ds_read_b128 v[190:193], v229 offset:1024
	ds_read_b128 v[194:197], v229 offset:2048
	ds_read_b128 v[198:201], v229 offset:3072
	global_load_lds_dwordx4 v[182:183], off
	v_lshl_add_u64 v[184:185], s[44:45], 0, v[218:219]
	s_mov_b32 m0, s60
	s_cselect_b32 s49, s52, s48
	global_load_lds_dwordx4 v[184:185], off
	s_barrier
	s_waitcnt lgkmcnt(0)
	s_cselect_b32 s48, s53, s28
	s_setprio 1
	s_waitcnt lgkmcnt(0)
	v_mfma_f32_16x16x32_f16 v[130:133], v[186:189], v[174:177], v[130:133]
	v_mfma_f32_16x16x32_f16 v[126:129], v[194:197], v[174:177], v[126:129]
	v_mfma_f32_16x16x32_f16 v[122:125], v[186:189], v[166:169], v[122:125]
	v_mfma_f32_16x16x32_f16 v[118:121], v[194:197], v[166:169], v[118:121]
	v_mfma_f32_16x16x32_f16 v[110:113], v[186:189], v[158:161], v[110:113]
	v_mfma_f32_16x16x32_f16 v[102:105], v[194:197], v[158:161], v[102:105]
	v_mfma_f32_16x16x32_f16 v[94:97], v[186:189], v[150:153], v[94:97]
	v_mfma_f32_16x16x32_f16 v[82:85], v[194:197], v[150:153], v[82:85]
	v_mfma_f32_16x16x32_f16 v[130:133], v[190:193], v[178:181], v[130:133]
	v_mfma_f32_16x16x32_f16 v[126:129], v[198:201], v[178:181], v[126:129]
	v_mfma_f32_16x16x32_f16 v[122:125], v[190:193], v[170:173], v[122:125]
	v_mfma_f32_16x16x32_f16 v[118:121], v[198:201], v[170:173], v[118:121]
	v_mfma_f32_16x16x32_f16 v[110:113], v[190:193], v[162:165], v[110:113]
	v_mfma_f32_16x16x32_f16 v[102:105], v[198:201], v[162:165], v[102:105]
	v_mfma_f32_16x16x32_f16 v[94:97], v[190:193], v[154:157], v[94:97]
	v_mfma_f32_16x16x32_f16 v[82:85], v[198:201], v[154:157], v[82:85]
	s_setprio 0
	s_mov_b32 m0, s58
	s_barrier
	ds_read_b128 v[150:153], v237 offset:16384
	ds_read_b128 v[154:157], v237 offset:17408
	ds_read_b128 v[158:161], v237 offset:18432
	ds_read_b128 v[162:165], v237 offset:19456
	ds_read_b128 v[166:169], v237 offset:20480
	ds_read_b128 v[170:173], v237 offset:21504
	ds_read_b128 v[174:177], v237 offset:22528
	ds_read_b128 v[178:181], v237 offset:23552
	global_load_lds_dwordx4 v220, s[48:49]
	s_mov_b32 m0, s62
	s_nop 0
	global_load_lds_dwordx4 v226, s[48:49]
	s_barrier
	s_waitcnt lgkmcnt(0)
	s_setprio 1
	s_waitcnt lgkmcnt(0)
	v_mfma_f32_16x16x32_f16 v[70:73], v[134:137], v[150:153], v[70:73]
	v_mfma_f32_16x16x32_f16 v[58:61], v[142:145], v[150:153], v[58:61]
	v_mfma_f32_16x16x32_f16 v[50:53], v[134:137], v[158:161], v[50:53]
	v_mfma_f32_16x16x32_f16 v[38:41], v[142:145], v[158:161], v[38:41]
	v_mfma_f32_16x16x32_f16 v[26:29], v[134:137], v[166:169], v[26:29]
	v_mfma_f32_16x16x32_f16 v[18:21], v[142:145], v[166:169], v[18:21]
	v_mfma_f32_16x16x32_f16 v[10:13], v[134:137], v[174:177], v[10:13]
	v_mfma_f32_16x16x32_f16 v[6:9], v[142:145], v[174:177], v[6:9]
	v_mfma_f32_16x16x32_f16 v[70:73], v[138:141], v[154:157], v[70:73]
	v_mfma_f32_16x16x32_f16 v[58:61], v[146:149], v[154:157], v[58:61]
	v_mfma_f32_16x16x32_f16 v[50:53], v[138:141], v[162:165], v[50:53]
	v_mfma_f32_16x16x32_f16 v[38:41], v[146:149], v[162:165], v[38:41]
	v_mfma_f32_16x16x32_f16 v[26:29], v[138:141], v[170:173], v[26:29]
	v_mfma_f32_16x16x32_f16 v[18:21], v[146:149], v[170:173], v[18:21]
	v_mfma_f32_16x16x32_f16 v[10:13], v[138:141], v[178:181], v[10:13]
	v_mfma_f32_16x16x32_f16 v[6:9], v[146:149], v[178:181], v[6:9]
	s_setprio 0
	s_barrier
	s_add_u32 s90, s44, 0x40000
	s_addc_u32 s91, s45, 0
	s_mov_b32 m0, s84
	v_lshl_add_u64 v[134:135], s[90:91], 0, v[216:217]
	global_load_lds_dwordx4 v[134:135], off
	v_lshl_add_u64 v[134:135], s[90:91], 0, v[218:219]
	s_mov_b32 m0, s85
	s_nop 0
	global_load_lds_dwordx4 v[134:135], off
	s_waitcnt vmcnt(6)
	s_barrier
	s_setprio 1
	v_mfma_f32_16x16x32_f16 v[90:93], v[186:189], v[150:153], v[90:93]
	v_mfma_f32_16x16x32_f16 v[78:81], v[194:197], v[150:153], v[78:81]
	v_mfma_f32_16x16x32_f16 v[66:69], v[186:189], v[158:161], v[66:69]
	v_mfma_f32_16x16x32_f16 v[54:57], v[194:197], v[158:161], v[54:57]
	v_mfma_f32_16x16x32_f16 v[42:45], v[186:189], v[166:169], v[42:45]
	v_mfma_f32_16x16x32_f16 v[30:33], v[194:197], v[166:169], v[30:33]
	v_mfma_f32_16x16x32_f16 v[22:25], v[186:189], v[174:177], v[22:25]
	v_mfma_f32_16x16x32_f16 v[14:17], v[194:197], v[174:177], v[14:17]
	v_mfma_f32_16x16x32_f16 v[90:93], v[190:193], v[154:157], v[90:93]
	v_mfma_f32_16x16x32_f16 v[78:81], v[198:201], v[154:157], v[78:81]
	v_mfma_f32_16x16x32_f16 v[66:69], v[190:193], v[162:165], v[66:69]
	v_mfma_f32_16x16x32_f16 v[54:57], v[198:201], v[162:165], v[54:57]
	v_mfma_f32_16x16x32_f16 v[42:45], v[190:193], v[170:173], v[42:45]
	v_mfma_f32_16x16x32_f16 v[30:33], v[198:201], v[170:173], v[30:33]
	v_mfma_f32_16x16x32_f16 v[22:25], v[190:193], v[178:181], v[22:25]
	v_mfma_f32_16x16x32_f16 v[14:17], v[198:201], v[178:181], v[14:17]
	s_setprio 0
	s_cmp_gt_i32 s61, 44
	s_cbranch_scc1 .Lhka_done_a2
	s_cmp_lt_i32 s61, 1
	s_cbranch_scc1 .Lhka_ld_a2
	s_add_i32 s94, s75, s61
	s_mov_b32 s95, 0
	s_cmpk_gt_u32 s94, 0x15ff
	s_cselect_b32 s97, 0x7fffea00, 0
	s_cselect_b32 s96, 0x80, 0
	s_add_i32 s97, s97, s94
	s_lshl_b32 s94, s97, 1
	s_add_i32 s97, s94, 0x2c00
	s_mul_hi_u32 s98, s97, 0xba2e8ba3
	s_lshr_b32 s98, s98, 11
	s_mul_i32 s99, s98, 0x7ffff500
	s_add_i32 s99, s99, s97
	s_lshr_b32 s97, s99, 7
	s_mul_i32 s98, s98, 22
	s_add_i32 s97, s97, s98
	s_lshl_b32 s97, s97, 8
	s_and_b32 s94, s94, 0x7e
	s_or_b32 s96, s97, s96
	s_or_b32 s94, s96, s94
	s_lshl_b64 s[96:97], s[94:95], 11
	v_cvt_pk_f16_f32 v2, v2, v3
	v_cvt_pk_f16_f32 v3, v4, v5
	v_lshl_add_u64 v[4:5], v[224:225], 0, s[96:97]
	global_store_dwordx2 v[4:5], v[2:3], off

.Lhka_done_a2:
	s_barrier
	ds_read_b128 v[134:137], v231
	ds_read_b128 v[138:141], v231 offset:1024
	ds_read_b128 v[142:145], v231 offset:2048
	ds_read_b128 v[146:149], v231 offset:3072
	s_mov_b32 m0, s63
	ds_read_b128 v[174:177], v237 offset:32768
	ds_read_b128 v[178:181], v237 offset:33792
	ds_read_b128 v[166:169], v237 offset:34816
	ds_read_b128 v[170:173], v237 offset:35840
	ds_read_b128 v[158:161], v237 offset:36864
	ds_read_b128 v[162:165], v237 offset:37888
	ds_read_b128 v[150:153], v237 offset:38912
	ds_read_b128 v[154:157], v237 offset:39936
	global_load_lds_dwordx4 v228, s[48:49]
	s_mov_b32 m0, s64
	s_nop 0
	global_load_lds_dwordx4 v230, s[48:49]
	s_waitcnt lgkmcnt(8)
	s_barrier
	s_waitcnt lgkmcnt(0)
	s_setprio 1
	s_waitcnt lgkmcnt(0)
	v_mfma_f32_16x16x32_f16 v[114:117], v[134:137], v[174:177], v[114:117]
	v_mfma_f32_16x16x32_f16 v[106:109], v[142:145], v[174:177], v[106:109]
	v_mfma_f32_16x16x32_f16 v[98:101], v[134:137], v[166:169], v[98:101]
	v_mfma_f32_16x16x32_f16 v[86:89], v[142:145], v[166:169], v[86:89]
	v_mfma_f32_16x16x32_f16 v[74:77], v[134:137], v[158:161], v[74:77]
	v_mfma_f32_16x16x32_f16 v[62:65], v[142:145], v[158:161], v[62:65]
	v_mfma_f32_16x16x32_f16 v[46:49], v[134:137], v[150:153], v[46:49]
	v_mfma_f32_16x16x32_f16 v[34:37], v[142:145], v[150:153], v[34:37]
	v_mfma_f32_16x16x32_f16 v[114:117], v[138:141], v[178:181], v[114:117]
	v_mfma_f32_16x16x32_f16 v[106:109], v[146:149], v[178:181], v[106:109]
	v_mfma_f32_16x16x32_f16 v[98:101], v[138:141], v[170:173], v[98:101]
	v_mfma_f32_16x16x32_f16 v[86:89], v[146:149], v[170:173], v[86:89]
	v_mfma_f32_16x16x32_f16 v[74:77], v[138:141], v[162:165], v[74:77]
	v_mfma_f32_16x16x32_f16 v[62:65], v[146:149], v[162:165], v[62:65]
	v_mfma_f32_16x16x32_f16 v[46:49], v[138:141], v[154:157], v[46:49]
	v_mfma_f32_16x16x32_f16 v[34:37], v[146:149], v[154:157], v[34:37]
	s_setprio 0
	s_barrier
.LBB4_46:
	s_mov_b32 m0, s67
	v_lshl_add_u64 v[182:183], v[182:183], 0, s[30:31]
	ds_read_b128 v[190:193], v238
	ds_read_b128 v[194:197], v238 offset:1024
	ds_read_b128 v[198:201], v238 offset:2048
	ds_read_b128 v[202:205], v238 offset:3072
	global_load_lds_dwordx4 v[182:183], off
	v_lshl_add_u64 v[182:183], v[184:185], 0, s[30:31]
	s_mov_b32 m0, s68
	v_mov_b32_e32 v227, v221
	global_load_lds_dwordx4 v[182:183], off
	s_barrier
	s_waitcnt lgkmcnt(0)
	v_lshl_add_u64 v[186:187], s[48:49], 0, v[220:221]
	v_lshl_add_u64 v[188:189], s[48:49], 0, v[226:227]
	s_setprio 1
	s_waitcnt lgkmcnt(0)
	v_mfma_f32_16x16x32_f16 v[130:133], v[190:193], v[174:177], v[130:133]
	v_mfma_f32_16x16x32_f16 v[126:129], v[198:201], v[174:177], v[126:129]
	v_mfma_f32_16x16x32_f16 v[122:125], v[190:193], v[166:169], v[122:125]
	v_mfma_f32_16x16x32_f16 v[118:121], v[198:201], v[166:169], v[118:121]
	v_mfma_f32_16x16x32_f16 v[110:113], v[190:193], v[158:161], v[110:113]
	v_mfma_f32_16x16x32_f16 v[102:105], v[198:201], v[158:161], v[102:105]
	v_mfma_f32_16x16x32_f16 v[94:97], v[190:193], v[150:153], v[94:97]
	v_mfma_f32_16x16x32_f16 v[82:85], v[198:201], v[150:153], v[82:85]
	v_mfma_f32_16x16x32_f16 v[130:133], v[194:197], v[178:181], v[130:133]
	v_mfma_f32_16x16x32_f16 v[126:129], v[202:205], v[178:181], v[126:129]
	v_mfma_f32_16x16x32_f16 v[122:125], v[194:197], v[170:173], v[122:125]
	v_mfma_f32_16x16x32_f16 v[118:121], v[202:205], v[170:173], v[118:121]
	v_mfma_f32_16x16x32_f16 v[110:113], v[194:197], v[162:165], v[110:113]
	v_mfma_f32_16x16x32_f16 v[102:105], v[202:205], v[162:165], v[102:105]
	v_mfma_f32_16x16x32_f16 v[94:97], v[194:197], v[154:157], v[94:97]
	v_mfma_f32_16x16x32_f16 v[82:85], v[202:205], v[154:157], v[82:85]
	s_setprio 0
	s_mov_b32 m0, s69
	v_lshl_add_u64 v[182:183], v[186:187], 0, s[30:31]
	s_barrier
	ds_read_b128 v[150:153], v237 offset:49152
	ds_read_b128 v[154:157], v237 offset:50176
	ds_read_b128 v[158:161], v237 offset:51200
	ds_read_b128 v[162:165], v237 offset:52224
	ds_read_b128 v[166:169], v237 offset:53248
	ds_read_b128 v[170:173], v237 offset:54272
	ds_read_b128 v[174:177], v237 offset:55296
	ds_read_b128 v[178:181], v237 offset:56320
	global_load_lds_dwordx4 v[182:183], off
	v_lshl_add_u64 v[182:183], v[188:189], 0, s[30:31]
	s_mov_b32 m0, s70
	s_nop 0
	global_load_lds_dwordx4 v[182:183], off
	s_barrier
	s_waitcnt lgkmcnt(0)
	s_setprio 1
	s_waitcnt lgkmcnt(0)
	v_mfma_f32_16x16x32_f16 v[70:73], v[134:137], v[150:153], v[70:73]
	v_mfma_f32_16x16x32_f16 v[58:61], v[142:145], v[150:153], v[58:61]
	v_mfma_f32_16x16x32_f16 v[50:53], v[134:137], v[158:161], v[50:53]
	v_mfma_f32_16x16x32_f16 v[38:41], v[142:145], v[158:161], v[38:41]
	v_mfma_f32_16x16x32_f16 v[26:29], v[134:137], v[166:169], v[26:29]
	v_mfma_f32_16x16x32_f16 v[18:21], v[142:145], v[166:169], v[18:21]
	v_mfma_f32_16x16x32_f16 v[10:13], v[134:137], v[174:177], v[10:13]
	v_mfma_f32_16x16x32_f16 v[6:9], v[142:145], v[174:177], v[6:9]
	v_mfma_f32_16x16x32_f16 v[70:73], v[138:141], v[154:157], v[70:73]
	v_mfma_f32_16x16x32_f16 v[58:61], v[146:149], v[154:157], v[58:61]
	v_mfma_f32_16x16x32_f16 v[50:53], v[138:141], v[162:165], v[50:53]
	v_mfma_f32_16x16x32_f16 v[38:41], v[146:149], v[162:165], v[38:41]
	v_mfma_f32_16x16x32_f16 v[26:29], v[138:141], v[170:173], v[26:29]
	v_mfma_f32_16x16x32_f16 v[18:21], v[146:149], v[170:173], v[18:21]
	v_mfma_f32_16x16x32_f16 v[10:13], v[138:141], v[178:181], v[10:13]
	v_mfma_f32_16x16x32_f16 v[6:9], v[146:149], v[178:181], v[6:9]
	s_setprio 0
	s_barrier
	s_add_u32 s44, s44, 0x40080
	s_addc_u32 s45, s45, 0
	s_mov_b32 m0, s50
	v_lshl_add_u64 v[134:135], s[44:45], 0, v[216:217]
	global_load_lds_dwordx4 v[134:135], off
	v_lshl_add_u64 v[134:135], s[44:45], 0, v[218:219]
	s_mov_b32 m0, s51
	s_nop 0
	global_load_lds_dwordx4 v[134:135], off
	s_waitcnt vmcnt(6)
	s_barrier
	s_setprio 1
	v_mfma_f32_16x16x32_f16 v[90:93], v[190:193], v[150:153], v[90:93]
	v_mfma_f32_16x16x32_f16 v[78:81], v[198:201], v[150:153], v[78:81]
	v_mfma_f32_16x16x32_f16 v[66:69], v[190:193], v[158:161], v[66:69]
	v_mfma_f32_16x16x32_f16 v[54:57], v[198:201], v[158:161], v[54:57]
	v_mfma_f32_16x16x32_f16 v[42:45], v[190:193], v[166:169], v[42:45]
	v_mfma_f32_16x16x32_f16 v[30:33], v[198:201], v[166:169], v[30:33]
	v_mfma_f32_16x16x32_f16 v[22:25], v[190:193], v[174:177], v[22:25]
	v_mfma_f32_16x16x32_f16 v[14:17], v[198:201], v[174:177], v[14:17]
	v_mfma_f32_16x16x32_f16 v[90:93], v[194:197], v[154:157], v[90:93]
	v_mfma_f32_16x16x32_f16 v[78:81], v[202:205], v[154:157], v[78:81]
	v_mfma_f32_16x16x32_f16 v[66:69], v[194:197], v[162:165], v[66:69]
	v_mfma_f32_16x16x32_f16 v[54:57], v[202:205], v[162:165], v[54:57]
	v_mfma_f32_16x16x32_f16 v[42:45], v[194:197], v[170:173], v[42:45]
	v_mfma_f32_16x16x32_f16 v[30:33], v[202:205], v[170:173], v[30:33]
	v_mfma_f32_16x16x32_f16 v[22:25], v[194:197], v[178:181], v[22:25]
	v_mfma_f32_16x16x32_f16 v[14:17], v[202:205], v[178:181], v[14:17]
	s_setprio 0
	s_cmp_gt_i32 s61, 44
	s_cbranch_scc1 .Lhka_done_a3
	s_cmp_lt_i32 s61, 1
	s_cbranch_scc1 .Lhka_ld_a3
	s_add_i32 s94, s75, s61
	s_mov_b32 s95, 0
	s_cmpk_gt_u32 s94, 0x15ff
	s_cselect_b32 s97, 0x7fffea00, 0
	s_cselect_b32 s96, 0x80, 0
	s_add_i32 s97, s97, s94
	s_lshl_b32 s94, s97, 1
	s_add_i32 s97, s94, 0x2c00
	s_mul_hi_u32 s98, s97, 0xba2e8ba3
	s_lshr_b32 s98, s98, 11
	s_mul_i32 s99, s98, 0x7ffff500
	s_add_i32 s99, s99, s97
	s_lshr_b32 s97, s99, 7
	s_mul_i32 s98, s98, 22
	s_add_i32 s97, s97, s98
	s_lshl_b32 s97, s97, 8
	s_and_b32 s94, s94, 0x7e
	s_or_b32 s96, s97, s96
	s_or_b32 s94, s96, s94
	s_lshl_b64 s[96:97], s[94:95], 11
	v_cvt_pk_f16_f32 v2, v2, v3
	v_cvt_pk_f16_f32 v3, v4, v5
	v_lshl_add_u64 v[4:5], v[224:225], 0, s[96:97]
	global_store_dwordx2 v[4:5], v[2:3], off

.Lhka_done_a3:
	s_add_i32 s28, s88, 2
	s_add_u32 s46, s46, 0x100
	s_addc_u32 s47, s47, 0
	s_add_u32 s86, s86, 0x100
	s_addc_u32 s87, s87, 0
	s_cmp_ge_i32 s88, s83
	s_barrier
	s_cbranch_scc1 .LBB4_49
	s_mov_b32 s88, s28
	s_branch .LBB4_32

.LBB5_18:
.LBB5_24:
	s_and_b64 s[46:47], s[38:39], exec
	s_cselect_b32 s48, s35, s43
	s_cselect_b32 s49, s34, s42
	s_cselect_b32 s50, s37, s41
	s_cselect_b32 s51, s36, s40
	s_add_u32 s24, s42, 0x100
	s_addc_u32 s80, s43, 0
	s_and_b64 s[46:47], s[44:45], exec
	s_cselect_b32 s47, s48, s80
	s_cselect_b32 s46, s49, s24
	s_add_u32 s24, s40, 0x100
	s_addc_u32 s80, s41, 0
	s_and_b64 s[44:45], s[44:45], exec
	s_cselect_b32 s45, s50, s80
	s_cselect_b32 s44, s51, s24
	s_mov_b32 m0, s55
	v_add_u32_e32 v227, s72, v232
	v_lshl_add_u64 v[130:131], s[44:45], 0, v[212:213]
	ds_read_b128 v[82:85], v227
	ds_read_b128 v[94:97], v227 offset:1024
	ds_read_b128 v[102:105], v227 offset:2048
	ds_read_b128 v[110:113], v227 offset:3072
	global_load_lds_dwordx4 v[130:131], off
	v_lshl_add_u64 v[132:133], s[44:45], 0, v[214:215]
	s_mov_b32 m0, s56
	s_nop 0
	global_load_lds_dwordx4 v[132:133], off
	s_barrier
	s_waitcnt lgkmcnt(0)
	s_setprio 1
	s_waitcnt lgkmcnt(0)
	v_mfma_f32_16x16x32_f16 v[90:93], v[82:85], v[46:49], 0
	v_mfma_f32_16x16x32_f16 v[46:49], v[102:105], v[46:49], 0
	v_mfma_f32_16x16x32_f16 v[90:93], v[94:97], v[50:53], v[90:93]
	v_mfma_f32_16x16x32_f16 v[46:49], v[110:113], v[50:53], v[46:49]
	v_mfma_f32_16x16x32_f16 v[50:53], v[82:85], v[38:41], 0
	v_mfma_f32_16x16x32_f16 v[38:41], v[102:105], v[38:41], 0
	v_mfma_f32_16x16x32_f16 v[106:109], v[110:113], v[42:45], v[38:41]
	v_mfma_f32_16x16x32_f16 v[38:41], v[82:85], v[30:33], 0
	v_mfma_f32_16x16x32_f16 v[30:33], v[102:105], v[30:33], 0
	v_mfma_f32_16x16x32_f16 v[170:173], v[110:113], v[34:37], v[30:33]
	v_mfma_f32_16x16x32_f16 v[30:33], v[82:85], v[22:25], 0
	v_mfma_f32_16x16x32_f16 v[22:25], v[102:105], v[22:25], 0
	v_mfma_f32_16x16x32_f16 v[98:101], v[94:97], v[42:45], v[50:53]
	v_mfma_f32_16x16x32_f16 v[166:169], v[94:97], v[34:37], v[38:41]
	v_mfma_f32_16x16x32_f16 v[174:177], v[94:97], v[26:29], v[30:33]
	v_mfma_f32_16x16x32_f16 v[178:181], v[110:113], v[26:29], v[22:25]
	s_setprio 0
	s_mov_b32 m0, s54
	s_barrier
	ds_read_b128 v[42:45], v235 offset:16384
	ds_read_b128 v[114:117], v235 offset:17408
	ds_read_b128 v[118:121], v235 offset:18432
	ds_read_b128 v[122:125], v235 offset:19456
	ds_read_b128 v[126:129], v235 offset:20480
	ds_read_b128 v[154:157], v235 offset:21504
	ds_read_b128 v[162:165], v235 offset:22528
	ds_read_b128 v[182:185], v235 offset:23552
	global_load_lds_dwordx4 v216, s[46:47]
	s_mov_b32 m0, s57
	s_nop 0
	global_load_lds_dwordx4 v222, s[46:47]
	s_barrier
	s_waitcnt lgkmcnt(0)
	s_setprio 1
	s_waitcnt lgkmcnt(0)
	v_mfma_f32_16x16x32_f16 v[22:25], v[6:9], v[42:45], 0
	v_mfma_f32_16x16x32_f16 v[30:33], v[6:9], v[118:121], 0
	v_mfma_f32_16x16x32_f16 v[38:41], v[6:9], v[126:129], 0
	v_mfma_f32_16x16x32_f16 v[6:9], v[6:9], v[162:165], 0
	v_mfma_f32_16x16x32_f16 v[22:25], v[10:13], v[114:117], v[22:25]
	v_mfma_f32_16x16x32_f16 v[26:29], v[14:17], v[42:45], 0
	v_mfma_f32_16x16x32_f16 v[30:33], v[10:13], v[122:125], v[30:33]
	v_mfma_f32_16x16x32_f16 v[34:37], v[14:17], v[118:121], 0
	v_mfma_f32_16x16x32_f16 v[38:41], v[10:13], v[154:157], v[38:41]
	v_mfma_f32_16x16x32_f16 v[50:53], v[14:17], v[126:129], 0
	v_mfma_f32_16x16x32_f16 v[6:9], v[10:13], v[182:185], v[6:9]
	v_mfma_f32_16x16x32_f16 v[10:13], v[14:17], v[162:165], 0
	v_mfma_f32_16x16x32_f16 v[26:29], v[18:21], v[114:117], v[26:29]
	v_mfma_f32_16x16x32_f16 v[34:37], v[18:21], v[122:125], v[34:37]
	v_mfma_f32_16x16x32_f16 v[50:53], v[18:21], v[154:157], v[50:53]
	v_mfma_f32_16x16x32_f16 v[14:17], v[18:21], v[182:185], v[10:13]
	s_setprio 0
	s_barrier
	s_add_u32 s82, s44, 0x40000
	s_addc_u32 s83, s45, 0
	s_add_i32 s80, s72, s53
	v_lshl_add_u64 v[10:11], s[82:83], 0, v[212:213]
	s_mov_b32 m0, s80
	s_add_i32 s81, s80, 0x2000
	global_load_lds_dwordx4 v[10:11], off
	v_lshl_add_u64 v[10:11], s[82:83], 0, v[214:215]
	s_mov_b32 m0, s81
	s_nop 0
	global_load_lds_dwordx4 v[10:11], off
	s_waitcnt vmcnt(6)
	s_barrier
	s_setprio 1
	v_mfma_f32_16x16x32_f16 v[10:13], v[82:85], v[42:45], 0
	v_mfma_f32_16x16x32_f16 v[134:137], v[94:97], v[114:117], v[10:13]
	v_mfma_f32_16x16x32_f16 v[10:13], v[102:105], v[42:45], 0
	v_mfma_f32_16x16x32_f16 v[138:141], v[110:113], v[114:117], v[10:13]
	v_mfma_f32_16x16x32_f16 v[10:13], v[82:85], v[118:121], 0
	v_mfma_f32_16x16x32_f16 v[142:145], v[94:97], v[122:125], v[10:13]
	v_mfma_f32_16x16x32_f16 v[10:13], v[102:105], v[118:121], 0
	v_mfma_f32_16x16x32_f16 v[146:149], v[110:113], v[122:125], v[10:13]
	v_mfma_f32_16x16x32_f16 v[10:13], v[82:85], v[126:129], 0
	v_mfma_f32_16x16x32_f16 v[150:153], v[94:97], v[154:157], v[10:13]
	v_mfma_f32_16x16x32_f16 v[10:13], v[102:105], v[126:129], 0
	v_mfma_f32_16x16x32_f16 v[154:157], v[110:113], v[154:157], v[10:13]
	v_mfma_f32_16x16x32_f16 v[10:13], v[82:85], v[162:165], 0
	v_mfma_f32_16x16x32_f16 v[158:161], v[94:97], v[182:185], v[10:13]
	v_mfma_f32_16x16x32_f16 v[10:13], v[102:105], v[162:165], 0
	v_mfma_f32_16x16x32_f16 v[162:165], v[110:113], v[182:185], v[10:13]
	s_setprio 0
	s_cmp_gt_i32 s63, 44
	s_cbranch_scc1 .Lhkb_done_b0
	s_cmp_lt_i32 s63, 1
	s_cbranch_scc1 .Lhkb_ld_b0
	s_add_i32 s92, s71, s63
	s_mov_b32 s93, 0
	s_lshl_b64 s[90:91], s[92:93], 12
	v_cvt_pk_f16_f32 v2, v2, v3
	v_cvt_pk_f16_f32 v3, v4, v5
	v_lshl_add_u64 v[4:5], v[220:221], 0, s[90:91]
	global_store_dwordx2 v[4:5], v[2:3], off

.Lhkb_done_b0:
	v_add_u32_e32 v229, 0x18000, v233
	s_barrier
	s_nop 3
	ds_read_b128 v[10:13], v229
	ds_read_b128 v[182:185], v229 offset:1024
	ds_read_b128 v[186:189], v229 offset:2048
	ds_read_b128 v[190:193], v229 offset:3072
	s_mov_b32 m0, s58
	ds_read_b128 v[122:125], v235 offset:32768
	ds_read_b128 v[126:129], v235 offset:33792
	ds_read_b128 v[114:117], v235 offset:34816
	ds_read_b128 v[206:209], v235 offset:35840
	ds_read_b128 v[198:201], v235 offset:36864
	ds_read_b128 v[202:205], v235 offset:37888
	ds_read_b128 v[18:21], v235 offset:38912
	ds_read_b128 v[194:197], v235 offset:39936
	global_load_lds_dwordx4 v226, s[46:47]
	s_mov_b32 m0, s59
	s_nop 0
	global_load_lds_dwordx4 v228, s[46:47]
	s_waitcnt lgkmcnt(8)
	s_barrier
	s_waitcnt lgkmcnt(0)
	s_setprio 1
	s_waitcnt lgkmcnt(0)
	v_mfma_f32_16x16x32_f16 v[42:45], v[10:13], v[122:125], v[54:57]
	v_mfma_f32_16x16x32_f16 v[118:121], v[182:185], v[126:129], v[42:45]
	v_mfma_f32_16x16x32_f16 v[42:45], v[186:189], v[122:125], v[58:61]
	v_mfma_f32_16x16x32_f16 v[110:113], v[190:193], v[126:129], v[42:45]
	v_mfma_f32_16x16x32_f16 v[42:45], v[10:13], v[114:117], v[62:65]
	v_mfma_f32_16x16x32_f16 v[102:105], v[182:185], v[206:209], v[42:45]
	v_mfma_f32_16x16x32_f16 v[42:45], v[186:189], v[114:117], v[66:69]
	v_mfma_f32_16x16x32_f16 v[94:97], v[190:193], v[206:209], v[42:45]
	v_mfma_f32_16x16x32_f16 v[42:45], v[10:13], v[198:201], v[70:73]
	v_mfma_f32_16x16x32_f16 v[82:85], v[182:185], v[202:205], v[42:45]
	v_mfma_f32_16x16x32_f16 v[42:45], v[186:189], v[198:201], v[74:77]
	v_mfma_f32_16x16x32_f16 v[66:69], v[190:193], v[202:205], v[42:45]
	v_mfma_f32_16x16x32_f16 v[42:45], v[10:13], v[18:21], v[78:81]
	v_mfma_f32_16x16x32_f16 v[54:57], v[182:185], v[194:197], v[42:45]
	v_mfma_f32_16x16x32_f16 v[42:45], v[186:189], v[18:21], v[86:89]
	v_mfma_f32_16x16x32_f16 v[42:45], v[190:193], v[194:197], v[42:45]
	s_setprio 0
	s_barrier
.LBB5_30:
	v_mov_b32_e32 v223, v217
	v_lshl_add_u64 v[58:59], s[46:47], 0, v[216:217]
	v_lshl_add_u64 v[60:61], s[46:47], 0, v[222:223]
	s_add_i32 s46, 0, 0x1c000
	s_mov_b32 m0, s62
	v_add_u32_e32 v236, s46, v232
	v_lshl_add_u64 v[62:63], v[130:131], 0, s[26:27]
	ds_read_b128 v[238:241], v236
	ds_read_b128 v[242:245], v236 offset:1024
	ds_read_b128 v[246:249], v236 offset:2048
	ds_read_b128 v[250:253], v236 offset:3072
	global_load_lds_dwordx4 v[62:63], off
	v_lshl_add_u64 v[62:63], v[132:133], 0, s[26:27]
	s_mov_b32 m0, s64
	s_nop 0
	global_load_lds_dwordx4 v[62:63], off
	s_barrier
	s_waitcnt lgkmcnt(0)
	s_setprio 1
	s_waitcnt lgkmcnt(0)
	v_mfma_f32_16x16x32_f16 v[62:65], v[238:241], v[122:125], v[90:93]
	v_mfma_f32_16x16x32_f16 v[46:49], v[246:249], v[122:125], v[46:49]
	v_mfma_f32_16x16x32_f16 v[130:133], v[242:245], v[126:129], v[62:65]
	v_mfma_f32_16x16x32_f16 v[126:129], v[250:253], v[126:129], v[46:49]
	v_mfma_f32_16x16x32_f16 v[46:49], v[238:241], v[114:117], v[98:101]
	v_mfma_f32_16x16x32_f16 v[122:125], v[242:245], v[206:209], v[46:49]
	v_mfma_f32_16x16x32_f16 v[46:49], v[246:249], v[114:117], v[106:109]
	v_mfma_f32_16x16x32_f16 v[114:117], v[250:253], v[206:209], v[46:49]
	v_mfma_f32_16x16x32_f16 v[46:49], v[238:241], v[198:201], v[166:169]
	v_mfma_f32_16x16x32_f16 v[106:109], v[242:245], v[202:205], v[46:49]
	v_mfma_f32_16x16x32_f16 v[46:49], v[246:249], v[198:201], v[170:173]
	v_mfma_f32_16x16x32_f16 v[98:101], v[250:253], v[202:205], v[46:49]
	v_mfma_f32_16x16x32_f16 v[46:49], v[238:241], v[18:21], v[174:177]
	v_mfma_f32_16x16x32_f16 v[18:21], v[246:249], v[18:21], v[178:181]
	v_mfma_f32_16x16x32_f16 v[90:93], v[242:245], v[194:197], v[46:49]
	v_mfma_f32_16x16x32_f16 v[78:81], v[250:253], v[194:197], v[18:21]
	s_setprio 0
	s_mov_b32 m0, s65
	s_nop 3
	v_lshl_add_u64 v[18:19], v[58:59], 0, s[26:27]
	s_barrier
	ds_read_b128 v[62:65], v235 offset:49152
	ds_read_b128 v[74:77], v235 offset:50176
	ds_read_b128 v[166:169], v235 offset:51200
	ds_read_b128 v[170:173], v235 offset:52224
	ds_read_b128 v[174:177], v235 offset:53248
	ds_read_b128 v[178:181], v235 offset:54272
	ds_read_b128 v[194:197], v235 offset:55296
	ds_read_b128 v[198:201], v235 offset:56320
	global_load_lds_dwordx4 v[18:19], off
	v_lshl_add_u64 v[18:19], v[60:61], 0, s[26:27]
	s_mov_b32 m0, s66
	s_nop 0
	global_load_lds_dwordx4 v[18:19], off
	s_barrier
	s_waitcnt lgkmcnt(0)
	s_setprio 1
	s_waitcnt lgkmcnt(0)
	v_mfma_f32_16x16x32_f16 v[18:21], v[10:13], v[62:65], v[22:25]
	v_mfma_f32_16x16x32_f16 v[70:73], v[182:185], v[74:77], v[18:21]
	v_mfma_f32_16x16x32_f16 v[18:21], v[186:189], v[62:65], v[26:29]
	v_mfma_f32_16x16x32_f16 v[58:61], v[190:193], v[74:77], v[18:21]
	v_mfma_f32_16x16x32_f16 v[18:21], v[10:13], v[166:169], v[30:33]
	v_mfma_f32_16x16x32_f16 v[46:49], v[182:185], v[170:173], v[18:21]
	v_mfma_f32_16x16x32_f16 v[18:21], v[186:189], v[166:169], v[34:37]
	v_mfma_f32_16x16x32_f16 v[34:37], v[190:193], v[170:173], v[18:21]
	v_mfma_f32_16x16x32_f16 v[18:21], v[10:13], v[174:177], v[38:41]
	v_mfma_f32_16x16x32_f16 v[6:9], v[10:13], v[194:197], v[6:9]
	v_mfma_f32_16x16x32_f16 v[26:29], v[182:185], v[178:181], v[18:21]
	v_mfma_f32_16x16x32_f16 v[18:21], v[186:189], v[174:177], v[50:53]
	v_mfma_f32_16x16x32_f16 v[10:13], v[182:185], v[198:201], v[6:9]
	v_mfma_f32_16x16x32_f16 v[6:9], v[186:189], v[194:197], v[14:17]
	v_mfma_f32_16x16x32_f16 v[18:21], v[190:193], v[178:181], v[18:21]
	v_mfma_f32_16x16x32_f16 v[6:9], v[190:193], v[198:201], v[6:9]
	s_setprio 0
	s_barrier
	s_add_u32 s44, s44, 0x40080
	s_addc_u32 s45, s45, 0
	s_add_i32 s46, s46, s53
	v_lshl_add_u64 v[14:15], s[44:45], 0, v[212:213]
	s_mov_b32 m0, s46
	s_add_i32 s47, s46, 0x2000
	global_load_lds_dwordx4 v[14:15], off
	v_lshl_add_u64 v[14:15], s[44:45], 0, v[214:215]
	s_mov_b32 m0, s47
	s_nop 0
	global_load_lds_dwordx4 v[14:15], off
	s_waitcnt vmcnt(6)
	s_barrier
	s_setprio 1
	v_mfma_f32_16x16x32_f16 v[14:17], v[238:241], v[62:65], v[134:137]
	v_mfma_f32_16x16x32_f16 v[86:89], v[242:245], v[74:77], v[14:17]
	v_mfma_f32_16x16x32_f16 v[14:17], v[246:249], v[62:65], v[138:141]
	v_mfma_f32_16x16x32_f16 v[74:77], v[250:253], v[74:77], v[14:17]
	v_mfma_f32_16x16x32_f16 v[14:17], v[238:241], v[166:169], v[142:145]
	v_mfma_f32_16x16x32_f16 v[62:65], v[242:245], v[170:173], v[14:17]
	v_mfma_f32_16x16x32_f16 v[14:17], v[246:249], v[166:169], v[146:149]
	v_mfma_f32_16x16x32_f16 v[50:53], v[250:253], v[170:173], v[14:17]
	v_mfma_f32_16x16x32_f16 v[14:17], v[238:241], v[174:177], v[150:153]
	v_mfma_f32_16x16x32_f16 v[38:41], v[242:245], v[178:181], v[14:17]
	v_mfma_f32_16x16x32_f16 v[14:17], v[246:249], v[174:177], v[154:157]
	v_mfma_f32_16x16x32_f16 v[30:33], v[250:253], v[178:181], v[14:17]
	v_mfma_f32_16x16x32_f16 v[14:17], v[238:241], v[194:197], v[158:161]
	v_mfma_f32_16x16x32_f16 v[22:25], v[242:245], v[198:201], v[14:17]
	v_mfma_f32_16x16x32_f16 v[14:17], v[246:249], v[194:197], v[162:165]
	v_mfma_f32_16x16x32_f16 v[14:17], v[250:253], v[198:201], v[14:17]
	s_setprio 0
	s_cmp_gt_i32 s63, 44
	s_cbranch_scc1 .Lhkb_done_b1
	s_cmp_lt_i32 s63, 1
	s_cbranch_scc1 .Lhkb_ld_b1
	s_add_i32 s92, s71, s63
	s_mov_b32 s93, 0
	s_lshl_b64 s[90:91], s[92:93], 12
	v_cvt_pk_f16_f32 v2, v2, v3
	v_cvt_pk_f16_f32 v3, v4, v5
	v_lshl_add_u64 v[4:5], v[220:221], 0, s[90:91]
	global_store_dwordx2 v[4:5], v[2:3], off

.Lhkb_done_b1:
	s_cmp_lt_u32 s79, 3
	s_barrier
	s_cbranch_scc1 .LBB5_49
	s_add_u32 s42, s42, 0x180
	s_addc_u32 s43, s43, 0
	s_add_u32 s82, s40, 0x200
	s_addc_u32 s83, s41, 0
	s_mov_b32 s84, 4

.LBB5_40:
	s_add_u32 s24, s42, 0x80
	s_addc_u32 s44, s43, 0
	s_and_b64 s[40:41], s[40:41], exec
	s_cselect_b32 s41, s50, s83
	s_cselect_b32 s40, s51, s82
	s_mov_b32 m0, s55
	v_lshl_add_u64 v[182:183], s[40:41], 0, v[212:213]
	ds_read_b128 v[186:189], v227
	ds_read_b128 v[190:193], v227 offset:1024
	ds_read_b128 v[194:197], v227 offset:2048
	ds_read_b128 v[198:201], v227 offset:3072
	global_load_lds_dwordx4 v[182:183], off
	v_lshl_add_u64 v[184:185], s[40:41], 0, v[214:215]
	s_mov_b32 m0, s56
	s_cselect_b32 s45, s48, s44
	global_load_lds_dwordx4 v[184:185], off
	s_barrier
	s_waitcnt lgkmcnt(0)
	s_cselect_b32 s44, s49, s24
	s_setprio 1
	s_waitcnt lgkmcnt(0)
	v_mfma_f32_16x16x32_f16 v[130:133], v[186:189], v[174:177], v[130:133]
	v_mfma_f32_16x16x32_f16 v[126:129], v[194:197], v[174:177], v[126:129]
	v_mfma_f32_16x16x32_f16 v[122:125], v[186:189], v[166:169], v[122:125]
	v_mfma_f32_16x16x32_f16 v[114:117], v[194:197], v[166:169], v[114:117]
	v_mfma_f32_16x16x32_f16 v[106:109], v[186:189], v[158:161], v[106:109]
	v_mfma_f32_16x16x32_f16 v[98:101], v[194:197], v[158:161], v[98:101]
	v_mfma_f32_16x16x32_f16 v[90:93], v[186:189], v[150:153], v[90:93]
	v_mfma_f32_16x16x32_f16 v[78:81], v[194:197], v[150:153], v[78:81]
	v_mfma_f32_16x16x32_f16 v[130:133], v[190:193], v[178:181], v[130:133]
	v_mfma_f32_16x16x32_f16 v[126:129], v[198:201], v[178:181], v[126:129]
	v_mfma_f32_16x16x32_f16 v[122:125], v[190:193], v[170:173], v[122:125]
	v_mfma_f32_16x16x32_f16 v[114:117], v[198:201], v[170:173], v[114:117]
	v_mfma_f32_16x16x32_f16 v[106:109], v[190:193], v[162:165], v[106:109]
	v_mfma_f32_16x16x32_f16 v[98:101], v[198:201], v[162:165], v[98:101]
	v_mfma_f32_16x16x32_f16 v[90:93], v[190:193], v[154:157], v[90:93]
	v_mfma_f32_16x16x32_f16 v[78:81], v[198:201], v[154:157], v[78:81]
	s_setprio 0
	s_mov_b32 m0, s54
	s_barrier
	ds_read_b128 v[150:153], v235 offset:16384
	ds_read_b128 v[154:157], v235 offset:17408
	ds_read_b128 v[158:161], v235 offset:18432
	ds_read_b128 v[162:165], v235 offset:19456
	ds_read_b128 v[166:169], v235 offset:20480
	ds_read_b128 v[170:173], v235 offset:21504
	ds_read_b128 v[174:177], v235 offset:22528
	ds_read_b128 v[178:181], v235 offset:23552
	global_load_lds_dwordx4 v216, s[44:45]
	s_mov_b32 m0, s57
	s_nop 0
	global_load_lds_dwordx4 v222, s[44:45]
	s_barrier
	s_waitcnt lgkmcnt(0)
	s_setprio 1
	s_waitcnt lgkmcnt(0)
	v_mfma_f32_16x16x32_f16 v[70:73], v[134:137], v[150:153], v[70:73]
	v_mfma_f32_16x16x32_f16 v[58:61], v[142:145], v[150:153], v[58:61]
	v_mfma_f32_16x16x32_f16 v[46:49], v[134:137], v[158:161], v[46:49]
	v_mfma_f32_16x16x32_f16 v[34:37], v[142:145], v[158:161], v[34:37]
	v_mfma_f32_16x16x32_f16 v[26:29], v[134:137], v[166:169], v[26:29]
	v_mfma_f32_16x16x32_f16 v[18:21], v[142:145], v[166:169], v[18:21]
	v_mfma_f32_16x16x32_f16 v[10:13], v[134:137], v[174:177], v[10:13]
	v_mfma_f32_16x16x32_f16 v[6:9], v[142:145], v[174:177], v[6:9]
	v_mfma_f32_16x16x32_f16 v[70:73], v[138:141], v[154:157], v[70:73]
	v_mfma_f32_16x16x32_f16 v[58:61], v[146:149], v[154:157], v[58:61]
	v_mfma_f32_16x16x32_f16 v[46:49], v[138:141], v[162:165], v[46:49]
	v_mfma_f32_16x16x32_f16 v[34:37], v[146:149], v[162:165], v[34:37]
	v_mfma_f32_16x16x32_f16 v[26:29], v[138:141], v[170:173], v[26:29]
	v_mfma_f32_16x16x32_f16 v[18:21], v[146:149], v[170:173], v[18:21]
	v_mfma_f32_16x16x32_f16 v[10:13], v[138:141], v[178:181], v[10:13]
	v_mfma_f32_16x16x32_f16 v[6:9], v[146:149], v[178:181], v[6:9]
	s_setprio 0
	s_barrier
	s_add_u32 s86, s40, 0x40000
	s_addc_u32 s87, s41, 0
	s_mov_b32 m0, s80
	v_lshl_add_u64 v[134:135], s[86:87], 0, v[212:213]
	global_load_lds_dwordx4 v[134:135], off
	v_lshl_add_u64 v[134:135], s[86:87], 0, v[214:215]
	s_mov_b32 m0, s81
	s_nop 0
	global_load_lds_dwordx4 v[134:135], off
	s_waitcnt vmcnt(6)
	s_barrier
	s_setprio 1
	v_mfma_f32_16x16x32_f16 v[86:89], v[186:189], v[150:153], v[86:89]
	v_mfma_f32_16x16x32_f16 v[74:77], v[194:197], v[150:153], v[74:77]
	v_mfma_f32_16x16x32_f16 v[62:65], v[186:189], v[158:161], v[62:65]
	v_mfma_f32_16x16x32_f16 v[50:53], v[194:197], v[158:161], v[50:53]
	v_mfma_f32_16x16x32_f16 v[38:41], v[186:189], v[166:169], v[38:41]
	v_mfma_f32_16x16x32_f16 v[30:33], v[194:197], v[166:169], v[30:33]
	v_mfma_f32_16x16x32_f16 v[22:25], v[186:189], v[174:177], v[22:25]
	v_mfma_f32_16x16x32_f16 v[14:17], v[194:197], v[174:177], v[14:17]
	v_mfma_f32_16x16x32_f16 v[86:89], v[190:193], v[154:157], v[86:89]
	v_mfma_f32_16x16x32_f16 v[74:77], v[198:201], v[154:157], v[74:77]
	v_mfma_f32_16x16x32_f16 v[62:65], v[190:193], v[162:165], v[62:65]
	v_mfma_f32_16x16x32_f16 v[50:53], v[198:201], v[162:165], v[50:53]
	v_mfma_f32_16x16x32_f16 v[38:41], v[190:193], v[170:173], v[38:41]
	v_mfma_f32_16x16x32_f16 v[30:33], v[198:201], v[170:173], v[30:33]
	v_mfma_f32_16x16x32_f16 v[22:25], v[190:193], v[178:181], v[22:25]
	v_mfma_f32_16x16x32_f16 v[14:17], v[198:201], v[178:181], v[14:17]
	s_setprio 0
	s_cmp_gt_i32 s63, 44
	s_cbranch_scc1 .Lhkb_done_b2
	s_cmp_lt_i32 s63, 1
	s_cbranch_scc1 .Lhkb_ld_b2
	s_add_i32 s92, s71, s63
	s_mov_b32 s93, 0
	s_lshl_b64 s[90:91], s[92:93], 12
	v_cvt_pk_f16_f32 v2, v2, v3
	v_cvt_pk_f16_f32 v3, v4, v5
	v_lshl_add_u64 v[4:5], v[220:221], 0, s[90:91]
	global_store_dwordx2 v[4:5], v[2:3], off

.Lhkb_done_b2:
	s_barrier
	ds_read_b128 v[134:137], v229
	ds_read_b128 v[138:141], v229 offset:1024
	ds_read_b128 v[142:145], v229 offset:2048
	ds_read_b128 v[146:149], v229 offset:3072
	s_mov_b32 m0, s58
	ds_read_b128 v[174:177], v235 offset:32768
	ds_read_b128 v[178:181], v235 offset:33792
	ds_read_b128 v[166:169], v235 offset:34816
	ds_read_b128 v[170:173], v235 offset:35840
	ds_read_b128 v[158:161], v235 offset:36864
	ds_read_b128 v[162:165], v235 offset:37888
	ds_read_b128 v[150:153], v235 offset:38912
	ds_read_b128 v[154:157], v235 offset:39936
	global_load_lds_dwordx4 v226, s[44:45]
	s_mov_b32 m0, s59
	s_nop 0
	global_load_lds_dwordx4 v228, s[44:45]
	s_waitcnt lgkmcnt(8)
	s_barrier
	s_waitcnt lgkmcnt(0)
	s_setprio 1
	s_waitcnt lgkmcnt(0)
	v_mfma_f32_16x16x32_f16 v[118:121], v[134:137], v[174:177], v[118:121]
	v_mfma_f32_16x16x32_f16 v[110:113], v[142:145], v[174:177], v[110:113]
	v_mfma_f32_16x16x32_f16 v[102:105], v[134:137], v[166:169], v[102:105]
	v_mfma_f32_16x16x32_f16 v[94:97], v[142:145], v[166:169], v[94:97]
	v_mfma_f32_16x16x32_f16 v[82:85], v[134:137], v[158:161], v[82:85]
	v_mfma_f32_16x16x32_f16 v[66:69], v[142:145], v[158:161], v[66:69]
	v_mfma_f32_16x16x32_f16 v[54:57], v[134:137], v[150:153], v[54:57]
	v_mfma_f32_16x16x32_f16 v[42:45], v[142:145], v[150:153], v[42:45]
	v_mfma_f32_16x16x32_f16 v[118:121], v[138:141], v[178:181], v[118:121]
	v_mfma_f32_16x16x32_f16 v[110:113], v[146:149], v[178:181], v[110:113]
	v_mfma_f32_16x16x32_f16 v[102:105], v[138:141], v[170:173], v[102:105]
	v_mfma_f32_16x16x32_f16 v[94:97], v[146:149], v[170:173], v[94:97]
	v_mfma_f32_16x16x32_f16 v[82:85], v[138:141], v[162:165], v[82:85]
	v_mfma_f32_16x16x32_f16 v[66:69], v[146:149], v[162:165], v[66:69]
	v_mfma_f32_16x16x32_f16 v[54:57], v[138:141], v[154:157], v[54:57]
	v_mfma_f32_16x16x32_f16 v[42:45], v[146:149], v[154:157], v[42:45]
	s_setprio 0
	s_barrier
.LBB5_46:
	s_mov_b32 m0, s62
	v_lshl_add_u64 v[182:183], v[182:183], 0, s[26:27]
	ds_read_b128 v[190:193], v236
	ds_read_b128 v[194:197], v236 offset:1024
	ds_read_b128 v[198:201], v236 offset:2048
	ds_read_b128 v[202:205], v236 offset:3072
	global_load_lds_dwordx4 v[182:183], off
	v_lshl_add_u64 v[182:183], v[184:185], 0, s[26:27]
	s_mov_b32 m0, s64
	v_mov_b32_e32 v223, v217
	global_load_lds_dwordx4 v[182:183], off
	s_barrier
	s_waitcnt lgkmcnt(0)
	v_lshl_add_u64 v[186:187], s[44:45], 0, v[216:217]
	v_lshl_add_u64 v[188:189], s[44:45], 0, v[222:223]
	s_setprio 1
	s_waitcnt lgkmcnt(0)
	v_mfma_f32_16x16x32_f16 v[130:133], v[190:193], v[174:177], v[130:133]
	v_mfma_f32_16x16x32_f16 v[126:129], v[198:201], v[174:177], v[126:129]
	v_mfma_f32_16x16x32_f16 v[122:125], v[190:193], v[166:169], v[122:125]
	v_mfma_f32_16x16x32_f16 v[114:117], v[198:201], v[166:169], v[114:117]
	v_mfma_f32_16x16x32_f16 v[106:109], v[190:193], v[158:161], v[106:109]
	v_mfma_f32_16x16x32_f16 v[98:101], v[198:201], v[158:161], v[98:101]
	v_mfma_f32_16x16x32_f16 v[90:93], v[190:193], v[150:153], v[90:93]
	v_mfma_f32_16x16x32_f16 v[78:81], v[198:201], v[150:153], v[78:81]
	v_mfma_f32_16x16x32_f16 v[130:133], v[194:197], v[178:181], v[130:133]
	v_mfma_f32_16x16x32_f16 v[126:129], v[202:205], v[178:181], v[126:129]
	v_mfma_f32_16x16x32_f16 v[122:125], v[194:197], v[170:173], v[122:125]
	v_mfma_f32_16x16x32_f16 v[114:117], v[202:205], v[170:173], v[114:117]
	v_mfma_f32_16x16x32_f16 v[106:109], v[194:197], v[162:165], v[106:109]
	v_mfma_f32_16x16x32_f16 v[98:101], v[202:205], v[162:165], v[98:101]
	v_mfma_f32_16x16x32_f16 v[90:93], v[194:197], v[154:157], v[90:93]
	v_mfma_f32_16x16x32_f16 v[78:81], v[202:205], v[154:157], v[78:81]
	s_setprio 0
	s_mov_b32 m0, s65
	v_lshl_add_u64 v[182:183], v[186:187], 0, s[26:27]
	s_barrier
	ds_read_b128 v[150:153], v235 offset:49152
	ds_read_b128 v[154:157], v235 offset:50176
	ds_read_b128 v[158:161], v235 offset:51200
	ds_read_b128 v[162:165], v235 offset:52224
	ds_read_b128 v[166:169], v235 offset:53248
	ds_read_b128 v[170:173], v235 offset:54272
	ds_read_b128 v[174:177], v235 offset:55296
	ds_read_b128 v[178:181], v235 offset:56320
	global_load_lds_dwordx4 v[182:183], off
	v_lshl_add_u64 v[182:183], v[188:189], 0, s[26:27]
	s_mov_b32 m0, s66
	s_nop 0
	global_load_lds_dwordx4 v[182:183], off
	s_barrier
	s_waitcnt lgkmcnt(0)
	s_setprio 1
	s_waitcnt lgkmcnt(0)
	v_mfma_f32_16x16x32_f16 v[70:73], v[134:137], v[150:153], v[70:73]
	v_mfma_f32_16x16x32_f16 v[58:61], v[142:145], v[150:153], v[58:61]
	v_mfma_f32_16x16x32_f16 v[46:49], v[134:137], v[158:161], v[46:49]
	v_mfma_f32_16x16x32_f16 v[34:37], v[142:145], v[158:161], v[34:37]
	v_mfma_f32_16x16x32_f16 v[26:29], v[134:137], v[166:169], v[26:29]
	v_mfma_f32_16x16x32_f16 v[18:21], v[142:145], v[166:169], v[18:21]
	v_mfma_f32_16x16x32_f16 v[10:13], v[134:137], v[174:177], v[10:13]
	v_mfma_f32_16x16x32_f16 v[6:9], v[142:145], v[174:177], v[6:9]
	v_mfma_f32_16x16x32_f16 v[70:73], v[138:141], v[154:157], v[70:73]
	v_mfma_f32_16x16x32_f16 v[58:61], v[146:149], v[154:157], v[58:61]
	v_mfma_f32_16x16x32_f16 v[46:49], v[138:141], v[162:165], v[46:49]
	v_mfma_f32_16x16x32_f16 v[34:37], v[146:149], v[162:165], v[34:37]
	v_mfma_f32_16x16x32_f16 v[26:29], v[138:141], v[170:173], v[26:29]
	v_mfma_f32_16x16x32_f16 v[18:21], v[146:149], v[170:173], v[18:21]
	v_mfma_f32_16x16x32_f16 v[10:13], v[138:141], v[178:181], v[10:13]
	v_mfma_f32_16x16x32_f16 v[6:9], v[146:149], v[178:181], v[6:9]
	s_setprio 0
	s_barrier
	s_add_u32 s40, s40, 0x40080
	s_addc_u32 s41, s41, 0
	s_mov_b32 m0, s46
	v_lshl_add_u64 v[134:135], s[40:41], 0, v[212:213]
	global_load_lds_dwordx4 v[134:135], off
	v_lshl_add_u64 v[134:135], s[40:41], 0, v[214:215]
	s_mov_b32 m0, s47
	s_nop 0
	global_load_lds_dwordx4 v[134:135], off
	s_waitcnt vmcnt(6)
	s_barrier
	s_setprio 1
	v_mfma_f32_16x16x32_f16 v[86:89], v[190:193], v[150:153], v[86:89]
	v_mfma_f32_16x16x32_f16 v[74:77], v[198:201], v[150:153], v[74:77]
	v_mfma_f32_16x16x32_f16 v[62:65], v[190:193], v[158:161], v[62:65]
	v_mfma_f32_16x16x32_f16 v[50:53], v[198:201], v[158:161], v[50:53]
	v_mfma_f32_16x16x32_f16 v[38:41], v[190:193], v[166:169], v[38:41]
	v_mfma_f32_16x16x32_f16 v[30:33], v[198:201], v[166:169], v[30:33]
	v_mfma_f32_16x16x32_f16 v[22:25], v[190:193], v[174:177], v[22:25]
	v_mfma_f32_16x16x32_f16 v[14:17], v[198:201], v[174:177], v[14:17]
	v_mfma_f32_16x16x32_f16 v[86:89], v[194:197], v[154:157], v[86:89]
	v_mfma_f32_16x16x32_f16 v[74:77], v[202:205], v[154:157], v[74:77]
	v_mfma_f32_16x16x32_f16 v[62:65], v[194:197], v[162:165], v[62:65]
	v_mfma_f32_16x16x32_f16 v[50:53], v[202:205], v[162:165], v[50:53]
	v_mfma_f32_16x16x32_f16 v[38:41], v[194:197], v[170:173], v[38:41]
	v_mfma_f32_16x16x32_f16 v[30:33], v[202:205], v[170:173], v[30:33]
	v_mfma_f32_16x16x32_f16 v[22:25], v[194:197], v[178:181], v[22:25]
	v_mfma_f32_16x16x32_f16 v[14:17], v[202:205], v[178:181], v[14:17]
	s_setprio 0
	s_cmp_gt_i32 s63, 44
	s_cbranch_scc1 .Lhkb_done_b3
	s_cmp_lt_i32 s63, 1
	s_cbranch_scc1 .Lhkb_ld_b3
	s_add_i32 s92, s71, s63
	s_mov_b32 s93, 0
	s_lshl_b64 s[90:91], s[92:93], 12
	v_cvt_pk_f16_f32 v2, v2, v3
	v_cvt_pk_f16_f32 v3, v4, v5
	v_lshl_add_u64 v[4:5], v[220:221], 0, s[90:91]
	global_store_dwordx2 v[4:5], v[2:3], off

.Lhkb_done_b3:
	s_add_i32 s24, s84, 2
	s_add_u32 s42, s42, 0x100
	s_addc_u32 s43, s43, 0
	s_add_u32 s82, s82, 0x100
	s_addc_u32 s83, s83, 0
	s_cmp_ge_i32 s84, s79
	s_barrier
	s_cbranch_scc1 .LBB5_49
	s_mov_b32 s84, s24
	s_branch .LBB5_32
